# P0 layer-0 pre-norm row loop: gain vector in VGPRs + next-row prefetch
# speedup vs baseline: 1.0173x; 1.0023x over previous
.LBB0_76:
	s_or_b64 exec, exec, s[4:5]
	v_readlane_b32 s8, v253, 0
	v_readlane_b32 s9, v253, 1
	s_mov_b64 s[6:7], s[8:9]
	v_mov_b32_e32 v1, v175
	v_readlane_b32 s2, v253, 8
	v_ashrrev_i32_e32 v0, 6, v1
	s_nop 0
	v_add_u32_e32 v0, s2, v0
	s_movk_i32 s2, 0x4000
	v_cmp_gt_i32_e32 vcc, s2, v0
	s_and_saveexec_b64 s[4:5], vcc
	s_cbranch_execz .LBB0_79
	s_load_dwordx2 s[2:3], s[8:9], 0x10
	s_load_dwordx2 s[10:11], s[6:7], 0x0
	v_and_b32_e32 v8, 63, v1
	v_ashrrev_i32_e32 v1, 31, v0
	v_lshlrev_b64 v[4:5], 11, v[0:1]
	v_readlane_b32 s12, v253, 2
	v_mov_b32_e32 v7, 0
	v_lshlrev_b32_e32 v6, 4, v8
	v_lshl_or_b32 v4, v8, 3, v4
	v_readlane_b32 s14, v253, 4
	v_readlane_b32 s15, v253, 5
	v_lshlrev_b64 v[8:9], 12, v[0:1]
	s_waitcnt lgkmcnt(0)
	v_lshl_add_u64 v[2:3], s[2:3], 0, v[6:7]
	v_lshl_add_u64 v[4:5], s[14:15], 0, v[4:5]
	s_mov_b64 s[2:3], 0x6640000
	v_or_b32_e32 v8, v8, v6
	v_lshl_add_u64 v[4:5], v[4:5], 0, s[2:3]
	s_ashr_i32 s87, s86, 31
	v_lshl_add_u64 v[6:7], s[10:11], 0, v[8:9]
	s_mov_b64 s[2:3], 0x800
	s_lshl_b64 s[6:7], s[86:87], 11
	v_lshl_add_u64 v[6:7], v[6:7], 0, s[2:3]
	s_lshl_b64 s[8:9], s[86:87], 12
	s_mov_b64 s[10:11], 0
	v_mov_b32_e32 v1, 0x358637bd
	s_mov_b32 s2, 0x800000
	s_movk_i32 s3, 0x3fff
	v_readlane_b32 s13, v253, 3
	global_load_dwordx4 v[60:63], v[2:3], off
	global_load_dwordx4 v[64:67], v[2:3], off offset:1024
	global_load_dwordx4 v[68:71], v[2:3], off offset:2048
	global_load_dwordx4 v[72:75], v[2:3], off offset:3072
	global_load_dwordx4 v[76:79], v[6:7], off offset:-2048
	global_load_dwordx4 v[80:83], v[6:7], off offset:-1024
	global_load_dwordx4 v[84:87], v[6:7], off
	global_load_dwordx4 v[88:91], v[6:7], off offset:1024
.LBB0_78:
	s_waitcnt vmcnt(0)
	v_mov_b32_e32 v8, v76
	v_mov_b32_e32 v9, v77
	v_mov_b32_e32 v10, v78
	v_mov_b32_e32 v11, v79
	v_mov_b32_e32 v12, v80
	v_mov_b32_e32 v13, v81
	v_mov_b32_e32 v14, v82
	v_mov_b32_e32 v15, v83
	v_mov_b32_e32 v16, v84
	v_mov_b32_e32 v17, v85
	v_mov_b32_e32 v18, v86
	v_mov_b32_e32 v19, v87
	v_mov_b32_e32 v20, v88
	v_mov_b32_e32 v21, v89
	v_mov_b32_e32 v22, v90
	v_mov_b32_e32 v23, v91
	v_mov_b64_e32 v[92:93], v[6:7]
	v_add_u32_e32 v0, s86, v0
	v_lshl_add_u64 v[6:7], v[6:7], 0, s[8:9]
	v_cmp_ge_i32_e32 vcc, s3, v0
	s_nop 1
	v_cndmask_b32_e32 v94, v92, v6, vcc
	v_cndmask_b32_e32 v95, v93, v7, vcc
	global_load_dwordx4 v[76:79], v[94:95], off offset:-2048
	global_load_dwordx4 v[80:83], v[94:95], off offset:-1024
	global_load_dwordx4 v[84:87], v[94:95], off
	global_load_dwordx4 v[88:91], v[94:95], off offset:1024
	v_mov_b32_e32 v34, v9
	v_mov_b32_e32 v35, v13
	v_mov_b32_e32 v32, v8
	v_mov_b32_e32 v33, v12
	v_mov_b32_e32 v42, v17
	v_mov_b32_e32 v43, v21
	v_pk_mul_f32 v[34:35], v[34:35], v[34:35]
	v_mov_b32_e32 v28, v10
	v_mov_b32_e32 v29, v14
	v_mov_b32_e32 v40, v16
	v_mov_b32_e32 v41, v20
	v_pk_mul_f32 v[42:43], v[42:43], v[42:43]
	v_pk_fma_f32 v[32:33], v[32:33], v[32:33], v[34:35]
	v_mov_b32_e32 v30, v11
	v_mov_b32_e32 v31, v15
	v_mov_b32_e32 v36, v18
	v_mov_b32_e32 v37, v22
	v_pk_fma_f32 v[34:35], v[40:41], v[40:41], v[42:43]
	v_pk_fma_f32 v[28:29], v[28:29], v[28:29], v[32:33]
	v_mov_b32_e32 v38, v19
	v_mov_b32_e32 v39, v23
	v_pk_fma_f32 v[32:33], v[36:37], v[36:37], v[34:35]
	v_pk_fma_f32 v[28:29], v[30:31], v[30:31], v[28:29]
	v_pk_fma_f32 v[30:31], v[38:39], v[38:39], v[32:33]
	v_add_f32_e32 v28, v28, v29
	v_add_f32_e32 v28, v28, v30
	v_add_f32_e32 v28, v28, v31
	ds_bpermute_b32 v29, v184, v28
	s_waitcnt lgkmcnt(0)
	v_add_f32_e32 v28, v28, v29
	ds_bpermute_b32 v29, v185, v28
	s_waitcnt lgkmcnt(0)
	v_add_f32_e32 v28, v28, v29
	ds_bpermute_b32 v29, v186, v28
	s_waitcnt lgkmcnt(0)
	v_add_f32_e32 v28, v28, v29
	ds_bpermute_b32 v29, v187, v28
	s_waitcnt lgkmcnt(0)
	v_add_f32_e32 v28, v28, v29
	ds_bpermute_b32 v29, v188, v28
	s_waitcnt lgkmcnt(0)
	v_add_f32_e32 v28, v28, v29
	ds_bpermute_b32 v29, v189, v28
	s_waitcnt lgkmcnt(0)
	v_add_f32_e32 v28, v28, v29
	v_fmamk_f32 v28, v28, 0x3a800000, v1
	v_mul_f32_e32 v29, 0x4b800000, v28
	v_cmp_gt_f32_e32 vcc, s2, v28
	s_nop 1
	v_cndmask_b32_e32 v28, v28, v29, vcc
	v_rsq_f32_e32 v28, v28
	s_nop 0
	v_mul_f32_e32 v29, 0x45800000, v28
	v_cndmask_b32_e32 v28, v28, v29, vcc
	v_pk_mul_f32 v[8:9], v[8:9], v[28:29] op_sel_hi:[1,0]
	v_pk_mul_f32 v[10:11], v[10:11], v[28:29] op_sel_hi:[1,0]
	v_pk_mul_f32 v[8:9], v[60:61], v[8:9]
	v_pk_mul_f32 v[10:11], v[62:63], v[10:11]
	v_cvt_pk_bf16_f32 v8, v8, v9
	v_cvt_pk_bf16_f32 v9, v10, v11
	global_store_dwordx2 v[4:5], v[8:9], off
	v_pk_mul_f32 v[12:13], v[12:13], v[28:29] op_sel_hi:[1,0]
	v_pk_mul_f32 v[14:15], v[14:15], v[28:29] op_sel_hi:[1,0]
	v_cmp_lt_i32_e32 vcc, s3, v0
	s_or_b64 s[10:11], vcc, s[10:11]
	v_pk_mul_f32 v[8:9], v[64:65], v[12:13]
	v_pk_mul_f32 v[10:11], v[66:67], v[14:15]
	v_cvt_pk_bf16_f32 v8, v8, v9
	v_cvt_pk_bf16_f32 v9, v10, v11
	global_store_dwordx2 v[4:5], v[8:9], off offset:512
	v_pk_mul_f32 v[12:13], v[16:17], v[28:29] op_sel_hi:[1,0]
	v_pk_mul_f32 v[14:15], v[18:19], v[28:29] op_sel_hi:[1,0]
	v_pk_mul_f32 v[8:9], v[12:13], v[68:69]
	v_pk_mul_f32 v[10:11], v[14:15], v[70:71]
	v_cvt_pk_bf16_f32 v8, v8, v9
	v_cvt_pk_bf16_f32 v9, v10, v11
	global_store_dwordx2 v[4:5], v[8:9], off offset:1024
	v_pk_mul_f32 v[12:13], v[20:21], v[28:29] op_sel_hi:[1,0]
	v_pk_mul_f32 v[14:15], v[22:23], v[28:29] op_sel_hi:[1,0]
	v_pk_mul_f32 v[8:9], v[12:13], v[72:73]
	v_pk_mul_f32 v[10:11], v[14:15], v[74:75]
	v_cvt_pk_bf16_f32 v8, v8, v9
	v_cvt_pk_bf16_f32 v9, v10, v11
	global_store_dwordx2 v[4:5], v[8:9], off offset:1536
	v_lshl_add_u64 v[4:5], v[4:5], 0, s[6:7]
	s_andn2_b64 exec, exec, s[10:11]
	s_cbranch_execnz .LBB0_78
